# stack1: early barrier invalidate, wave0 x rows in barrier 1, NA first window all rows in flight, P5 gather merged, P5 tiles balanced over XCDs
# speedup vs baseline: 1.0044x; 1.0044x over previous
; DEVINL unsigned xb_ld(unsigned* p)              { return __hip_atomic_load(p, __ATOMIC_RELAXED, __HIP_MEMORY_SCOPE_AGENT); }
; DEVINL unsigned xb_add(unsigned* p, unsigned v) { return __hip_atomic_fetch_add(p, v, __ATOMIC_RELAXED, __HIP_MEMORY_SCOPE_AGENT); }
; #define XB_SPIN(cond, bar) do { unsigned _sp = 0; while (cond) { __builtin_amdgcn_s_sleep(1); \
;     if ((++_sp & 255u) == 0u) { if (xb_ld(&(bar)[XB_TMO])) break; if (_sp > XB_SPIN_CAP) { atomicAdd(&(bar)[XB_TMO], 1u); break; } } } } while (0)
; DEVINL void stage_x_load(const Params& P, int m0, XPre& X) {
;     const int wv = __builtin_amdgcn_readfirstlane(threadIdx.x >> 6); int lane = threadIdx.x & 63; asm volatile("" : "+v"(lane));
; #pragma unroll
;     for (int rr = 0; rr < 8; ++rr) {
;         const f32x4* xr = (const f32x4*)(P.x + (size_t)(m0 + 8 * wv + rr) * DM) + lane;
; #pragma unroll
;         for (int j = 0; j < 4; ++j) X.v[rr][j] = __builtin_nontemporal_load(xr + 64 * j);
;     }
; }
; template <int W> DEVINL void xcd_barrier_w(const XcdBarrier& b, const Params& P, XPre& X) {
;     ...
;     if (threadIdx.x == 0) {
;         unsigned* bar = b.bar;
;         __builtin_amdgcn_s_waitcnt(0);
;         unsigned nloc = b.st[0], nx = b.st[1];
;         const unsigned old = xb_add(&bar[XB_XSUBI((W - 1), b.x)], 1u);
;         if (nloc == 0u) { xcd_barrier_complete(bar, b.x, nloc, nx); b.st[0] = nloc; b.st[1] = nx; }
;         if (old + 1u == nloc) {
;             __builtin_amdgcn_fence(__ATOMIC_RELEASE, "agent");
;             asm volatile("s_waitcnt vmcnt(0)" ::: "memory");
;             (void)xb_add(&bar[XB_TOPI((W - 1))], 1u);
;         }
;         XB_SPIN(xb_ld(&bar[XB_TOPI((W - 1))]) < nx, bar);
.LBB0_154:
	s_or_b64 exec, exec, s[4:5]
	buffer_inv sc1
	s_mov_b64 s[12:13], exec
	s_mov_b64 exec, -1
	s_load_dwordx2 s[14:15], s[96:97], 0x0
	v_and_b32_e32 v2, 63, v0
	s_lshl_b32 s16, s80, 18
	v_lshlrev_b32_e32 v2, 4, v2
	s_waitcnt lgkmcnt(0)
	s_add_u32 s14, s14, s16
	s_addc_u32 s15, s15, 0
	global_load_dwordx4 v[126:129], v2, s[14:15] nt
	global_load_dwordx4 v[122:125], v2, s[14:15] offset:1024 nt
	global_load_dwordx4 v[118:121], v2, s[14:15] offset:2048 nt
	global_load_dwordx4 v[114:117], v2, s[14:15] offset:3072 nt
	s_add_u32 s14, s14, 0x1000
	s_addc_u32 s15, s15, 0
	global_load_dwordx4 v[110:113], v2, s[14:15] nt
	global_load_dwordx4 v[106:109], v2, s[14:15] offset:1024 nt
	global_load_dwordx4 v[102:105], v2, s[14:15] offset:2048 nt
	global_load_dwordx4 v[98:101], v2, s[14:15] offset:3072 nt
	s_add_u32 s14, s14, 0x1000
	s_addc_u32 s15, s15, 0
	global_load_dwordx4 v[94:97], v2, s[14:15] nt
	global_load_dwordx4 v[90:93], v2, s[14:15] offset:1024 nt
	global_load_dwordx4 v[86:89], v2, s[14:15] offset:2048 nt
	global_load_dwordx4 v[82:85], v2, s[14:15] offset:3072 nt
	s_add_u32 s14, s14, 0x1000
	s_addc_u32 s15, s15, 0
	global_load_dwordx4 v[78:81], v2, s[14:15] nt
	global_load_dwordx4 v[74:77], v2, s[14:15] offset:1024 nt
	global_load_dwordx4 v[70:73], v2, s[14:15] offset:2048 nt
	global_load_dwordx4 v[66:69], v2, s[14:15] offset:3072 nt
	s_add_u32 s14, s14, 0x1000
	s_addc_u32 s15, s15, 0
	global_load_dwordx4 v[62:65], v2, s[14:15] nt
	global_load_dwordx4 v[58:61], v2, s[14:15] offset:1024 nt
	global_load_dwordx4 v[54:57], v2, s[14:15] offset:2048 nt
	global_load_dwordx4 v[50:53], v2, s[14:15] offset:3072 nt
	s_add_u32 s14, s14, 0x1000
	s_addc_u32 s15, s15, 0
	global_load_dwordx4 v[46:49], v2, s[14:15] nt
	global_load_dwordx4 v[42:45], v2, s[14:15] offset:1024 nt
	global_load_dwordx4 v[38:41], v2, s[14:15] offset:2048 nt
	global_load_dwordx4 v[34:37], v2, s[14:15] offset:3072 nt
	s_add_u32 s14, s14, 0x1000
	s_addc_u32 s15, s15, 0
	global_load_dwordx4 v[30:33], v2, s[14:15] nt
	global_load_dwordx4 v[22:25], v2, s[14:15] offset:1024 nt
	global_load_dwordx4 v[18:21], v2, s[14:15] offset:2048 nt
	global_load_dwordx4 v[10:13], v2, s[14:15] offset:3072 nt
	s_add_u32 s14, s14, 0x1000
	s_addc_u32 s15, s15, 0
	global_load_dwordx4 v[26:29], v2, s[14:15] nt
	global_load_dwordx4 v[14:17], v2, s[14:15] offset:1024 nt
	global_load_dwordx4 v[6:9], v2, s[14:15] offset:2048 nt
	global_load_dwordx4 v[2:5], v2, s[14:15] offset:3072 nt
	s_mov_b64 exec, s[12:13]
	v_mov_b32_e32 v1, 0
	s_getpc_b64 s[2:3]
	s_add_u32 s2, s2, g_xbar@rel32@lo+32772
	s_addc_u32 s3, s3, g_xbar@rel32@hi+32780
	global_load_dword v131, v1, s[2:3] sc1
	s_waitcnt vmcnt(0) lgkmcnt(0)
	v_cmp_ge_u32_e32 vcc, v131, v130
	s_cbranch_vccnz .LBB0_167
	s_mov_b32 s2, 1
	s_branch .LBB0_157

; DEVINL unsigned xb_ld(unsigned* p)              { return __hip_atomic_load(p, __ATOMIC_RELAXED, __HIP_MEMORY_SCOPE_AGENT); }
; #define XB_SPIN(cond, bar) do { unsigned _sp = 0; while (cond) { __builtin_amdgcn_s_sleep(1); \
;     if ((++_sp & 255u) == 0u) { if (xb_ld(&(bar)[XB_TMO])) break; if (_sp > XB_SPIN_CAP) { atomicAdd(&(bar)[XB_TMO], 1u); break; } } } } while (0)
; template <int W> DEVINL void xcd_barrier_w(const XcdBarrier& b, const Params& P, XPre& X) {
;     ...
;         XB_SPIN(xb_ld(&bar[XB_TOPI((W - 1))]) < nx, bar);
;         __builtin_amdgcn_fence(__ATOMIC_ACQUIRE, "agent");
;         asm volatile("s_waitcnt vmcnt(0)" ::: "memory");
.LBB0_167:
	s_waitcnt vmcnt(0)
	s_waitcnt vmcnt(0)

; DEVINL void phase2(const Params& P, unsigned char* smem, XPre& X, const bool have_pre) {
;     if ((!have_pre || threadIdx.x < 64) && (int)blockIdx.x < NT / 64) stage_x_load(P, (int)blockIdx.x * 64, X);
.LBB0_171:
	s_cmp_lt_i32 s76, 2
	s_cselect_b64 s[2:3], -1, 0
	s_cmp_gt_i32 s77, 1
	s_cselect_b64 s[0:1], -1, 0
	v_writelane_b32 v254, s2, 40
	s_and_b64 s[0:1], s[2:3], s[0:1]
	s_andn2_b64 vcc, exec, s[0:1]
	v_writelane_b32 v254, s3, 41
	v_cmp_gt_u32_e64 s[6:7], 64, v0
	s_cbranch_vccnz .LBB0_331
	v_readlane_b32 s0, v254, 22
	v_readlane_b32 s1, v254, 23
	s_or_b64 s[2:3], s[0:1], s[6:7]
	s_cmpk_lt_i32 s80, 0x100
	s_cselect_b64 s[0:1], -1, 0
	s_and_b64 s[2:3], s[0:1], s[2:3]
	s_mov_b64 s[4:5], exec

; DEVINL unsigned xb_ld(unsigned* p)              { return __hip_atomic_load(p, __ATOMIC_RELAXED, __HIP_MEMORY_SCOPE_AGENT); }
; DEVINL unsigned xb_add(unsigned* p, unsigned v) { return __hip_atomic_fetch_add(p, v, __ATOMIC_RELAXED, __HIP_MEMORY_SCOPE_AGENT); }
; #define XB_SPIN(cond, bar) do { unsigned _sp = 0; while (cond) { __builtin_amdgcn_s_sleep(1); \
;     if ((++_sp & 255u) == 0u) { if (xb_ld(&(bar)[XB_TMO])) break; if (_sp > XB_SPIN_CAP) { atomicAdd(&(bar)[XB_TMO], 1u); break; } } } } while (0)
; template <int W> DEVINL void xcd_barrier_w(const XcdBarrier& b, const Params& P, XPre& X) {
;     ...
;     if (threadIdx.x == 0) {
;         unsigned* bar = b.bar;
;         __builtin_amdgcn_s_waitcnt(0);
;         unsigned nloc = b.st[0], nx = b.st[1];
;         const unsigned old = xb_add(&bar[XB_XSUBI((W - 1), b.x)], 1u);
;         if (nloc == 0u) { xcd_barrier_complete(bar, b.x, nloc, nx); b.st[0] = nloc; b.st[1] = nx; }
;         if (old + 1u == nloc) {
;             __builtin_amdgcn_fence(__ATOMIC_RELEASE, "agent");
;             asm volatile("s_waitcnt vmcnt(0)" ::: "memory");
;             (void)xb_add(&bar[XB_TOPI((W - 1))], 1u);
;         }
;         XB_SPIN(xb_ld(&bar[XB_TOPI((W - 1))]) < nx, bar);
.LBB0_428:
	s_or_b64 exec, exec, s[4:5]
	buffer_inv sc1
	v_mov_b32_e32 v1, 0
	s_getpc_b64 s[2:3]
	s_add_u32 s2, s2, g_xbar@rel32@lo+33028
	s_addc_u32 s3, s3, g_xbar@rel32@hi+33036
	global_load_dword v3, v1, s[2:3] sc1
	s_waitcnt vmcnt(0) lgkmcnt(0)
	v_cmp_ge_u32_e32 vcc, v3, v2
	s_cbranch_vccnz .LBB0_441
	s_mov_b32 s2, 1
	s_branch .LBB0_431

; DEVINL void xb_st0(unsigned* p) { __hip_atomic_store(p, 0u, __ATOMIC_RELAXED, __HIP_MEMORY_SCOPE_AGENT); }
; DEVINL void xb_reset_after(unsigned* bar, int i) {
; #pragma unroll
;     for (int j = 0; j < 16; ++j) xb_st0(&bar[XB_XSUBI(i - 1, j)]);
;     xb_st0(&bar[XB_TOPI(i - 1)]);
;     if (i == 1) {
; #pragma unroll
;         for (int j = 0; j < 16; ++j) xb_st0(&bar[256 + 64 * j]);
;     }
; }
; template <int W> DEVINL void xcd_barrier_w(const XcdBarrier& b, const Params& P, XPre& X) {
;     ...
;         __builtin_amdgcn_fence(__ATOMIC_ACQUIRE, "agent");
;         asm volatile("s_waitcnt vmcnt(0)" ::: "memory");
;         if (blockIdx.x == 0 && (W - 1) >= 1) xb_reset_after(bar, (W - 1));
.LBB0_441:
	s_waitcnt vmcnt(0)
	v_readlane_b32 s2, v254, 2
	s_waitcnt vmcnt(0)
	v_readlane_b32 s3, v254, 3
	s_andn2_b64 vcc, exec, s[2:3]
	s_cbranch_vccnz .LBB0_443
	s_getpc_b64 s[2:3]
	s_add_u32 s2, s2, g_xbar@rel32@lo+16388
	s_addc_u32 s3, s3, g_xbar@rel32@hi+16396
	v_mov_b32_e32 v1, 0
	global_store_dword v1, v1, s[2:3] sc1
	s_getpc_b64 s[2:3]
	s_add_u32 s2, s2, g_xbar@rel32@lo+16644
	s_addc_u32 s3, s3, g_xbar@rel32@hi+16652
	global_store_dword v1, v1, s[2:3] sc1
	s_getpc_b64 s[2:3]
	s_add_u32 s2, s2, g_xbar@rel32@lo+16900
	s_addc_u32 s3, s3, g_xbar@rel32@hi+16908
	global_store_dword v1, v1, s[2:3] sc1
	s_getpc_b64 s[2:3]
	s_add_u32 s2, s2, g_xbar@rel32@lo+17156
	s_addc_u32 s3, s3, g_xbar@rel32@hi+17164
	global_store_dword v1, v1, s[2:3] sc1
	s_getpc_b64 s[2:3]
	s_add_u32 s2, s2, g_xbar@rel32@lo+17412
	s_addc_u32 s3, s3, g_xbar@rel32@hi+17420
	global_store_dword v1, v1, s[2:3] sc1
	s_getpc_b64 s[2:3]
	s_add_u32 s2, s2, g_xbar@rel32@lo+17668
	s_addc_u32 s3, s3, g_xbar@rel32@hi+17676
	global_store_dword v1, v1, s[2:3] sc1
	s_getpc_b64 s[2:3]
	s_add_u32 s2, s2, g_xbar@rel32@lo+17924
	s_addc_u32 s3, s3, g_xbar@rel32@hi+17932
	global_store_dword v1, v1, s[2:3] sc1
	s_getpc_b64 s[2:3]
	s_add_u32 s2, s2, g_xbar@rel32@lo+18180
	s_addc_u32 s3, s3, g_xbar@rel32@hi+18188
	global_store_dword v1, v1, s[2:3] sc1
	s_getpc_b64 s[2:3]
	s_add_u32 s2, s2, g_xbar@rel32@lo+18436
	s_addc_u32 s3, s3, g_xbar@rel32@hi+18444
	global_store_dword v1, v1, s[2:3] sc1
	s_getpc_b64 s[2:3]
	s_add_u32 s2, s2, g_xbar@rel32@lo+18692
	s_addc_u32 s3, s3, g_xbar@rel32@hi+18700
	global_store_dword v1, v1, s[2:3] sc1
	s_getpc_b64 s[2:3]
	s_add_u32 s2, s2, g_xbar@rel32@lo+18948
	s_addc_u32 s3, s3, g_xbar@rel32@hi+18956
	global_store_dword v1, v1, s[2:3] sc1
	s_getpc_b64 s[2:3]
	s_add_u32 s2, s2, g_xbar@rel32@lo+19204
	s_addc_u32 s3, s3, g_xbar@rel32@hi+19212
	global_store_dword v1, v1, s[2:3] sc1
	s_getpc_b64 s[2:3]
	s_add_u32 s2, s2, g_xbar@rel32@lo+19460
	s_addc_u32 s3, s3, g_xbar@rel32@hi+19468
	global_store_dword v1, v1, s[2:3] sc1
	s_getpc_b64 s[2:3]
	s_add_u32 s2, s2, g_xbar@rel32@lo+19716
	s_addc_u32 s3, s3, g_xbar@rel32@hi+19724
	global_store_dword v1, v1, s[2:3] sc1
	s_getpc_b64 s[2:3]
	s_add_u32 s2, s2, g_xbar@rel32@lo+19972
	s_addc_u32 s3, s3, g_xbar@rel32@hi+19980
	global_store_dword v1, v1, s[2:3] sc1
	s_getpc_b64 s[2:3]
	s_add_u32 s2, s2, g_xbar@rel32@lo+20228
	s_addc_u32 s3, s3, g_xbar@rel32@hi+20236
	global_store_dword v1, v1, s[2:3] sc1
	s_getpc_b64 s[2:3]
	s_add_u32 s2, s2, g_xbar@rel32@lo+32772
	s_addc_u32 s3, s3, g_xbar@rel32@hi+32780
	global_store_dword v1, v1, s[2:3] sc1
	s_getpc_b64 s[2:3]
	s_add_u32 s2, s2, g_xbar@rel32@lo+1028
	s_addc_u32 s3, s3, g_xbar@rel32@hi+1036
	global_store_dword v1, v1, s[2:3] sc1
	s_getpc_b64 s[2:3]
	s_add_u32 s2, s2, g_xbar@rel32@lo+1284
	s_addc_u32 s3, s3, g_xbar@rel32@hi+1292
	global_store_dword v1, v1, s[2:3] sc1
	s_getpc_b64 s[2:3]
	s_add_u32 s2, s2, g_xbar@rel32@lo+1540
	s_addc_u32 s3, s3, g_xbar@rel32@hi+1548
	global_store_dword v1, v1, s[2:3] sc1
	s_getpc_b64 s[2:3]
	s_add_u32 s2, s2, g_xbar@rel32@lo+1796
	s_addc_u32 s3, s3, g_xbar@rel32@hi+1804
	global_store_dword v1, v1, s[2:3] sc1
	s_getpc_b64 s[2:3]
	s_add_u32 s2, s2, g_xbar@rel32@lo+2052
	s_addc_u32 s3, s3, g_xbar@rel32@hi+2060
	global_store_dword v1, v1, s[2:3] sc1
	s_getpc_b64 s[2:3]
	s_add_u32 s2, s2, g_xbar@rel32@lo+2308
	s_addc_u32 s3, s3, g_xbar@rel32@hi+2316
	global_store_dword v1, v1, s[2:3] sc1
	s_getpc_b64 s[2:3]
	s_add_u32 s2, s2, g_xbar@rel32@lo+2564
	s_addc_u32 s3, s3, g_xbar@rel32@hi+2572
	global_store_dword v1, v1, s[2:3] sc1
	s_getpc_b64 s[2:3]
	s_add_u32 s2, s2, g_xbar@rel32@lo+2820
	s_addc_u32 s3, s3, g_xbar@rel32@hi+2828
	global_store_dword v1, v1, s[2:3] sc1
	s_getpc_b64 s[2:3]
	s_add_u32 s2, s2, g_xbar@rel32@lo+3076
	s_addc_u32 s3, s3, g_xbar@rel32@hi+3084
	global_store_dword v1, v1, s[2:3] sc1
	s_getpc_b64 s[2:3]
	s_add_u32 s2, s2, g_xbar@rel32@lo+3332
	s_addc_u32 s3, s3, g_xbar@rel32@hi+3340
	global_store_dword v1, v1, s[2:3] sc1
	s_getpc_b64 s[2:3]
	s_add_u32 s2, s2, g_xbar@rel32@lo+3588
	s_addc_u32 s3, s3, g_xbar@rel32@hi+3596
	global_store_dword v1, v1, s[2:3] sc1
	s_getpc_b64 s[2:3]
	s_add_u32 s2, s2, g_xbar@rel32@lo+3844
	s_addc_u32 s3, s3, g_xbar@rel32@hi+3852
	global_store_dword v1, v1, s[2:3] sc1
	s_getpc_b64 s[2:3]
	s_add_u32 s2, s2, g_xbar@rel32@lo+4100
	s_addc_u32 s3, s3, g_xbar@rel32@hi+4108
	global_store_dword v1, v1, s[2:3] sc1
	s_getpc_b64 s[2:3]
	s_add_u32 s2, s2, g_xbar@rel32@lo+4356
	s_addc_u32 s3, s3, g_xbar@rel32@hi+4364
	global_store_dword v1, v1, s[2:3] sc1
	s_getpc_b64 s[2:3]
	s_add_u32 s2, s2, g_xbar@rel32@lo+4612
	s_addc_u32 s3, s3, g_xbar@rel32@hi+4620
	global_store_dword v1, v1, s[2:3] sc1
	s_getpc_b64 s[2:3]
	s_add_u32 s2, s2, g_xbar@rel32@lo+4868
	s_addc_u32 s3, s3, g_xbar@rel32@hi+4876
	global_store_dword v1, v1, s[2:3] sc1

; DEVINL void phase3(const Params& P, unsigned char* smem) {
;     ...
;         for (int i = t; i < 465; i += NTHR) s_rpb[i] = P.na_rpb[h * 465 + i] * LOG2E;
;         {
;             const int lo = R0OF(R0), hi = R0OF(R0 + 1) + 7;
;             for (int row = lo; row <= hi; ++row) {
;                 const u32x4 kk_ = *(const u32x4*)(Kg + (size_t)row * 4096 + t * 8), vv_ = *(const u32x4*)(Vg + (size_t)row * 4096 + t * 8);
;                 const int sl = (row % 9) * 8192;
;                 *(u32x4*)(smem + KR + sl + k_off(t >> 3, t & 7)) = kk_; *(u32x4*)(smem + VR + sl + v_off(t >> 3, t & 7)) = vv_;
;             }
.LBB0_455:
	s_bfe_u32 s8, s79, 0x30004
	s_waitcnt vmcnt(4)
	v_mov_b32_e32 v94, v1
	s_barrier
	s_and_saveexec_b64 s[0:1], s[6:7]
	s_cbranch_execz .LBB0_457
	s_mul_i32 s9, s8, 0x1d1
	v_readlane_b32 s80, v254, 4
	s_waitcnt vmcnt(2)
	v_add_lshl_u32 v86, s9, v0, 2
	v_readlane_b32 s92, v254, 16
	v_readlane_b32 s93, v254, 17
	s_mov_b32 s80, s44
	v_readlane_b32 s81, v254, 5
	v_readlane_b32 s82, v254, 6
	v_readlane_b32 s83, v254, 7
	v_readlane_b32 s84, v254, 8
	global_load_dword v251, v86, s[92:93]
	v_readlane_b32 s85, v254, 9
	v_readlane_b32 s86, v254, 10
	v_readlane_b32 s87, v254, 11
	v_readlane_b32 s88, v254, 12
	v_readlane_b32 s89, v254, 13
	v_readlane_b32 s90, v254, 14
	v_readlane_b32 s91, v254, 15
	v_readlane_b32 s94, v254, 18
	v_readlane_b32 s95, v254, 19
.LBB0_457:
	s_or_b64 exec, exec, s[0:1]
	s_and_b32 s81, s79, 15
	s_lshr_b32 s0, s79, 4
	s_ashr_i32 s9, s79, 7
	s_lshl_b32 s10, s81, 3
	s_and_b32 s30, s0, 7
	s_lshl_b32 s11, s9, 3
	s_add_i32 s0, s10, -4
	s_or_b32 s1, s10, 4
	s_cmp_eq_u32 s81, 0
	s_cselect_b32 s0, 0, s0
	s_cselect_b32 s12, 7, s1
	s_cmp_gt_i32 s0, s12
	s_cbranch_scc1 .LBB0_460
	s_add_i32 s14, s11, s30
	s_ashr_i32 s15, s14, 31
	s_ashr_i32 s1, s0, 31
	s_lshl_b64 s[14:15], s[14:15], 20
	s_lshl_b64 s[16:17], s[0:1], 13
	s_add_u32 s14, s14, s16
	s_addc_u32 s15, s15, s17
	s_waitcnt vmcnt(2)
	v_lshl_add_u64 v[86:87], v[186:187], 0, s[14:15]
	s_mul_hi_i32 s1, s0, 0x38e38e39
	s_lshr_b32 s16, s1, 31
	s_lshr_b32 s1, s1, 1
	s_add_i32 s1, s1, s16
	s_mul_i32 s1, s1, 9
	s_sub_i32 s1, s0, s1
	s_lshl_b32 s1, s1, 13
	s_mov_b64 s[14:15], 0x2000
	s_add_i32 s13, s0, 8
	s_cmp_gt_i32 s13, s12
	s_cbranch_scc1 .Lna_w_no9a
	s_mov_b64 s[16:17], 0x10000
	v_lshl_add_u64 v[88:89], v[86:87], 0, s[16:17]
	s_nop 0
	v_add_co_u32_e32 v92, vcc, 0x1000000, v88
	global_load_dwordx4 v[54:57], v[88:89], off
	s_nop 0
	v_addc_co_u32_e32 v93, vcc, 0, v89, vcc
	global_load_dwordx4 v[230:233], v[92:93], off
.Lna_w_no9a:
	v_add_co_u32_e32 v92, vcc, 0x1000000, v86
	global_load_dwordx4 v[22:25], v[86:87], off
	s_nop 0
	v_addc_co_u32_e32 v93, vcc, 0, v87, vcc
	global_load_dwordx4 v[58:61], v[92:93], off
	v_lshl_add_u64 v[86:87], v[86:87], 0, s[14:15]
	v_add_co_u32_e32 v92, vcc, 0x1000000, v86
	global_load_dwordx4 v[26:29], v[86:87], off
	s_nop 0
	v_addc_co_u32_e32 v93, vcc, 0, v87, vcc
	global_load_dwordx4 v[62:65], v[92:93], off
	v_lshl_add_u64 v[86:87], v[86:87], 0, s[14:15]
	v_add_co_u32_e32 v92, vcc, 0x1000000, v86
	global_load_dwordx4 v[30:33], v[86:87], off
	s_nop 0
	v_addc_co_u32_e32 v93, vcc, 0, v87, vcc
	global_load_dwordx4 v[66:69], v[92:93], off
	v_lshl_add_u64 v[86:87], v[86:87], 0, s[14:15]
	v_add_co_u32_e32 v92, vcc, 0x1000000, v86
	global_load_dwordx4 v[34:37], v[86:87], off
	s_nop 0
	v_addc_co_u32_e32 v93, vcc, 0, v87, vcc
	global_load_dwordx4 v[70:73], v[92:93], off
	v_lshl_add_u64 v[86:87], v[86:87], 0, s[14:15]
	v_add_co_u32_e32 v92, vcc, 0x1000000, v86
	global_load_dwordx4 v[38:41], v[86:87], off
	s_nop 0
	v_addc_co_u32_e32 v93, vcc, 0, v87, vcc
	global_load_dwordx4 v[74:77], v[92:93], off
	v_lshl_add_u64 v[86:87], v[86:87], 0, s[14:15]
	v_add_co_u32_e32 v92, vcc, 0x1000000, v86
	global_load_dwordx4 v[42:45], v[86:87], off
	s_nop 0
	v_addc_co_u32_e32 v93, vcc, 0, v87, vcc
	global_load_dwordx4 v[78:81], v[92:93], off
	v_lshl_add_u64 v[86:87], v[86:87], 0, s[14:15]
	v_add_co_u32_e32 v92, vcc, 0x1000000, v86
	global_load_dwordx4 v[46:49], v[86:87], off
	s_nop 0
	v_addc_co_u32_e32 v93, vcc, 0, v87, vcc
	global_load_dwordx4 v[82:85], v[92:93], off
	v_lshl_add_u64 v[86:87], v[86:87], 0, s[14:15]
	v_add_co_u32_e32 v92, vcc, 0x1000000, v86
	global_load_dwordx4 v[50:53], v[86:87], off
	s_nop 0
	v_addc_co_u32_e32 v93, vcc, 0, v87, vcc
	global_load_dwordx4 v[226:229], v[92:93], off
	v_add_u32_e32 v92, s1, v203
	v_add_u32_e32 v93, s1, v204
	s_add_i32 s1, s1, 0x2000
	s_cmp_eq_u32 s1, 0x12000
	s_cselect_b32 s1, 0, s1
	s_waitcnt vmcnt(15)
	ds_write_b128 v92, v[22:25]
	s_waitcnt vmcnt(14)
	ds_write_b128 v93, v[58:61]
	v_add_u32_e32 v92, s1, v203
	v_add_u32_e32 v93, s1, v204
	s_add_i32 s1, s1, 0x2000
	s_cmp_eq_u32 s1, 0x12000
	s_cselect_b32 s1, 0, s1
	s_waitcnt vmcnt(13)
	ds_write_b128 v92, v[26:29]
	s_waitcnt vmcnt(12)
	ds_write_b128 v93, v[62:65]
	v_add_u32_e32 v92, s1, v203
	v_add_u32_e32 v93, s1, v204
	s_add_i32 s1, s1, 0x2000
	s_cmp_eq_u32 s1, 0x12000
	s_cselect_b32 s1, 0, s1
	s_waitcnt vmcnt(11)
	ds_write_b128 v92, v[30:33]
	s_waitcnt vmcnt(10)
	ds_write_b128 v93, v[66:69]
	v_add_u32_e32 v92, s1, v203
	v_add_u32_e32 v93, s1, v204
	s_add_i32 s1, s1, 0x2000
	s_cmp_eq_u32 s1, 0x12000
	s_cselect_b32 s1, 0, s1
	s_waitcnt vmcnt(9)
	ds_write_b128 v92, v[34:37]
	s_waitcnt vmcnt(8)
	ds_write_b128 v93, v[70:73]
	v_add_u32_e32 v92, s1, v203
	v_add_u32_e32 v93, s1, v204
	s_add_i32 s1, s1, 0x2000
	s_cmp_eq_u32 s1, 0x12000
	s_cselect_b32 s1, 0, s1
	s_waitcnt vmcnt(7)
	ds_write_b128 v92, v[38:41]
	s_waitcnt vmcnt(6)
	ds_write_b128 v93, v[74:77]
	v_add_u32_e32 v92, s1, v203
	v_add_u32_e32 v93, s1, v204
	s_add_i32 s1, s1, 0x2000
	s_cmp_eq_u32 s1, 0x12000
	s_cselect_b32 s1, 0, s1
	s_waitcnt vmcnt(5)
	ds_write_b128 v92, v[42:45]
	s_waitcnt vmcnt(4)
	ds_write_b128 v93, v[78:81]
	v_add_u32_e32 v92, s1, v203
	v_add_u32_e32 v93, s1, v204
	s_add_i32 s1, s1, 0x2000
	s_cmp_eq_u32 s1, 0x12000
	s_cselect_b32 s1, 0, s1
	s_waitcnt vmcnt(3)
	ds_write_b128 v92, v[46:49]
	s_waitcnt vmcnt(2)
	ds_write_b128 v93, v[82:85]
	v_add_u32_e32 v92, s1, v203
	v_add_u32_e32 v93, s1, v204
	s_add_i32 s1, s1, 0x2000
	s_cmp_eq_u32 s1, 0x12000
	s_cselect_b32 s1, 0, s1
	s_waitcnt vmcnt(1)
	ds_write_b128 v92, v[50:53]
	s_waitcnt vmcnt(0)
	ds_write_b128 v93, v[226:229]
	s_cmp_gt_i32 s13, s12
	s_cbranch_scc1 .Lna_w_no9b
	v_add_u32_e32 v92, s1, v203
	v_add_u32_e32 v93, s1, v204
	ds_write_b128 v92, v[54:57]
	ds_write_b128 v93, v[230:233]
; DEVINL void phase3(const Params& P, unsigned char* smem) {
;     ...
;         for (int i = t; i < 465; i += NTHR) s_rpb[i] = P.na_rpb[h * 465 + i] * LOG2E;
;         {
;             const int lo = R0OF(R0), hi = R0OF(R0 + 1) + 7;
;             for (int row = lo; row <= hi; ++row) {
;                 const u32x4 kk_ = *(const u32x4*)(Kg + (size_t)row * 4096 + t * 8), vv_ = *(const u32x4*)(Vg + (size_t)row * 4096 + t * 8);
;                 const int sl = (row % 9) * 8192;
;                 *(u32x4*)(smem + KR + sl + k_off(t >> 3, t & 7)) = kk_; *(u32x4*)(smem + VR + sl + v_off(t >> 3, t & 7)) = vv_;
;             }
;         }
;         f32x4 bia[16];
;         const bool edge = grp == 0 || grp == 15;
;         bf16x8 qn0, qn1;
;         { const bf16_t* qp = Qg + (size_t)((R0 + rs) * 64 + c0 + lr) * 64 + 8 * g; qn0 = *(const bf16x8*)qp; qn1 = *(const bf16x8*)(qp + 32); }
; #pragma unroll 1
;         for (int p = 0; p < 4; ++p) {
;             const int r = R0 + 2 * p + rs, r0 = R0OF(r);
;             const int hi_p = R0OF(R0 + 2 * p + 1) + 7, hi_n = p < 3 ? R0OF(R0 + 2 * p + 3) + 7 : hi_p;
;             __syncthreads();
;             const bf16x8 q0 = qn0, q1 = qn1;
;             if (p == 0 || edge) {
;                 const int c = c0 + lr; int cs = c - 8; cs = cs < 0 ? 0 : (cs > 48 ? 48 : cs);
;                 const float* rp = s_rpb + (r0 - r + 7) * 31;
; #pragma unroll
;                 for (int j = 0; j < 8; ++j) {
;                     const int kc = kc0 + (j >> 2) * 16 + 4 * g + (j & 3);
;                     const bool ok = (kc >= cs) && (kc < cs + 16);
;                     int dc = kc - c + 15; dc = dc < 0 ? 0 : (dc > 30 ? 30 : dc);
.Lna_w_no9b:
.LBB0_460:
	s_waitcnt vmcnt(0)
	s_and_saveexec_b64 s[0:1], s[6:7]
	v_mul_f32_e32 v251, 0x3fb8aa3b, v251
	ds_write_b32 v205, v251
	s_or_b64 exec, exec, s[0:1]
	s_and_b32 s0, s78, 15
	s_lshl_b32 s82, s0, 3
	s_lshl_b32 s48, s0, 9
	s_or_b32 s0, s11, s8
	s_ashr_i32 s1, s0, 31
	s_add_i32 s83, s55, s82
	s_sub_i32 s84, s77, s82
	s_lshl_b64 s[0:1], s[0:1], 20
	s_add_u32 s12, s58, s0
	s_addc_u32 s13, s59, s1
	s_add_u32 s14, s60, s0
	s_addc_u32 s15, s61, s1
	s_add_u32 s0, s62, s0
	s_addc_u32 s1, s63, s1
	s_add_i32 s10, s10, s55
	s_lshl_b32 s10, s10, 6
	v_and_b32_e32 v95, 15, v94
	v_ashrrev_i32_e32 v98, 4, v94
	s_or_b32 s10, s10, s56
	v_or_b32_e32 v174, s10, v95
	s_waitcnt vmcnt(2)
	v_lshlrev_b32_e32 v88, 3, v98
	v_lshlrev_b64 v[86:87], 7, v[174:175]
	v_ashrrev_i32_e32 v89, 31, v88
	v_lshl_add_u64 v[86:87], s[12:13], 0, v[86:87]
	v_lshlrev_b64 v[96:97], 1, v[88:89]
	v_lshl_add_u64 v[86:87], v[86:87], 0, v[96:97]
	global_load_dwordx4 v[90:93], v[86:87], off
	s_nop 0
	global_load_dwordx4 v[86:89], v[86:87], off offset:64
	v_or_b32_e32 v208, s56, v95
	v_lshl_add_u64 v[190:191], s[12:13], 0, v[96:97]
	v_med3_i32 v96, v208, 8, 56
	v_lshlrev_b32_e32 v97, 2, v98
	v_add_u32_e32 v100, -8, v96
	v_add_u32_e32 v101, v97, v202
	v_add_u32_e32 v102, 8, v96
	v_bfe_u32 v96, v94, 2, 2
	v_mov_b32_e32 v189, v175
	v_or_b32_e32 v103, v101, v96
	v_lshlrev_b32_e32 v96, 3, v94
	s_add_i32 s79, s79, s2
	v_lshl_add_u64 v[194:195], s[0:1], 0, v[188:189]
	v_and_b32_e32 v96, 24, v96
	v_lshl_add_u32 v104, v103, 7, 0
	s_mov_b32 s0, 0x12000
	s_cmpk_gt_i32 s79, 0xff
	v_lshl_add_u64 v[192:193], s[14:15], 0, v[188:189]
	v_add3_u32 v189, v104, v96, s0
	s_cselect_b64 s[38:39], -1, 0
	s_lshl_b32 s49, s9, 13
	s_lshl_b32 s0, s8, 7
	v_sub_u32_e32 v105, v101, v208
	s_add_u32 s0, s26, s0
	v_cmp_ge_i32_e32 vcc, v101, v100
	v_cmp_lt_i32_e64 s[10:11], v101, v102
	v_med3_i32 v209, v105, -15, 15
	v_or_b32_e32 v105, 1, v101
	s_addc_u32 s1, s27, 0
	s_and_b64 s[10:11], vcc, s[10:11]
	v_cmp_ge_i32_e32 vcc, v105, v100
	v_cmp_lt_i32_e64 s[12:13], v105, v102
	v_sub_u32_e32 v105, v105, v208
	v_med3_i32 v210, v105, -15, 15
	v_or_b32_e32 v105, 2, v101
	s_and_b64 s[12:13], vcc, s[12:13]
	v_cmp_ge_i32_e32 vcc, v105, v100
	v_cmp_lt_i32_e64 s[14:15], v105, v102
	v_sub_u32_e32 v105, v105, v208
	v_med3_i32 v211, v105, -15, 15
	v_or_b32_e32 v105, 3, v101
	s_and_b64 s[14:15], vcc, s[14:15]
	v_cmp_ge_i32_e32 vcc, v105, v100
	v_cmp_lt_i32_e64 s[16:17], v105, v102
	v_sub_u32_e32 v105, v105, v208
	v_and_b32_e32 v104, 16, v94
	v_cmp_gt_u32_e64 s[8:9], 16, v94
	v_med3_i32 v212, v105, -15, 15
	v_add_u32_e32 v105, 16, v101
	v_add_u16_e32 v94, v94, v202
	v_add_u32_e32 v99, 4, v98
	v_and_b32_e32 v96, -8, v97
	s_and_b64 s[16:17], vcc, s[16:17]
	v_cmp_ge_i32_e32 vcc, v105, v100
	v_cmp_lt_i32_e64 s[18:19], v105, v102
	v_sub_u32_e32 v105, v105, v208
	v_lshrrev_b16_e32 v94, 1, v94
	v_ashrrev_i32_e32 v97, 31, v96
	v_med3_i32 v213, v105, -15, 15
	v_add_u32_e32 v105, 17, v101
	v_bitop3_b32 v98, v94, v98, 7 bitop3:0x6c
	v_bitop3_b32 v94, v94, v99, 7 bitop3:0x6c
	v_lshl_add_u64 v[96:97], v[96:97], 1, s[0:1]
	s_and_b64 s[18:19], vcc, s[18:19]
	v_cmp_ge_i32_e32 vcc, v105, v100
	v_cmp_lt_i32_e64 s[20:21], v105, v102
	v_sub_u32_e32 v105, v105, v208
	v_lshlrev_b32_e32 v219, 4, v94
	v_lshlrev_b32_e32 v94, 4, v103
	s_movk_i32 s0, 0x60
	v_med3_i32 v214, v105, -15, 15
	v_add_u32_e32 v105, 18, v101
	v_bitop3_b32 v223, v94, s0, v94 bitop3:0xc
	s_add_i32 s0, s76, s49
	s_and_b64 s[20:21], vcc, s[20:21]
	v_cmp_ge_i32_e32 vcc, v105, v100
	v_cmp_lt_i32_e64 s[22:23], v105, v102
	v_add_u32_e32 v101, 19, v101
	s_add_i32 s0, s0, s48
	s_and_b64 s[22:23], vcc, s[22:23]
	v_sub_u32_e32 v105, v105, v208
	v_cmp_ge_i32_e32 vcc, v101, v100
	v_cmp_lt_i32_e64 s[24:25], v101, v102
	v_sub_u32_e32 v100, v101, v208
	v_lshlrev_b32_e32 v174, 1, v104
	v_add_u32_e32 v198, s0, v95
	v_med3_i32 v215, v105, -15, 15
	s_and_b64 s[24:25], vcc, s[24:25]
	v_med3_i32 v216, v100, -15, 15
	v_add_lshl_u32 v217, v95, v202, 7
	v_lshlrev_b32_e32 v218, 4, v98
	v_and_b32_e32 v220, 0x60, v94
	v_bitop3_b32 v221, v94, 32, v206 bitop3:0x6c
	v_bitop3_b32 v222, v94, 64, v206 bitop3:0x6c
	v_lshl_add_u64 v[196:197], v[96:97], 0, v[174:175]
	v_lshl_or_b32 v200, v198, 4, s30
	s_mov_b32 s85, 0
	s_branch .LBB0_462

; DEVINL unsigned xb_ld(unsigned* p)              { return __hip_atomic_load(p, __ATOMIC_RELAXED, __HIP_MEMORY_SCOPE_AGENT); }
; DEVINL unsigned xb_add(unsigned* p, unsigned v) { return __hip_atomic_fetch_add(p, v, __ATOMIC_RELAXED, __HIP_MEMORY_SCOPE_AGENT); }
; #define XB_SPIN(cond, bar) do { unsigned _sp = 0; while (cond) { __builtin_amdgcn_s_sleep(1); \
;     if ((++_sp & 255u) == 0u) { if (xb_ld(&(bar)[XB_TMO])) break; if (_sp > XB_SPIN_CAP) { atomicAdd(&(bar)[XB_TMO], 1u); break; } } } } while (0)
; template <int W> DEVINL void xcd_barrier_w(const XcdBarrier& b, const Params& P, XPre& X) {
;     ...
;     if (threadIdx.x == 0) {
;         unsigned* bar = b.bar;
;         __builtin_amdgcn_s_waitcnt(0);
;         unsigned nloc = b.st[0], nx = b.st[1];
;         const unsigned old = xb_add(&bar[XB_XSUBI((W - 1), b.x)], 1u);
;         if (nloc == 0u) { xcd_barrier_complete(bar, b.x, nloc, nx); b.st[0] = nloc; b.st[1] = nx; }
;         if (old + 1u == nloc) {
;             __builtin_amdgcn_fence(__ATOMIC_RELEASE, "agent");
;             asm volatile("s_waitcnt vmcnt(0)" ::: "memory");
;             (void)xb_add(&bar[XB_TOPI((W - 1))], 1u);
;         }
;         XB_SPIN(xb_ld(&bar[XB_TOPI((W - 1))]) < nx, bar);
.LBB0_557:
	s_or_b64 exec, exec, s[4:5]
	buffer_inv sc1
	v_mov_b32_e32 v1, 0
	s_getpc_b64 s[2:3]
	s_add_u32 s2, s2, g_xbar@rel32@lo+33284
	s_addc_u32 s3, s3, g_xbar@rel32@hi+33292
	global_load_dword v3, v1, s[2:3] sc1
	s_waitcnt vmcnt(0) lgkmcnt(0)
	v_cmp_ge_u32_e32 vcc, v3, v2
	s_cbranch_vccnz .LBB0_570
	s_mov_b32 s2, 1
	s_branch .LBB0_560

; DEVINL void xb_st0(unsigned* p) { __hip_atomic_store(p, 0u, __ATOMIC_RELAXED, __HIP_MEMORY_SCOPE_AGENT); }
; DEVINL void xb_reset_after(unsigned* bar, int i) {
; #pragma unroll
;     for (int j = 0; j < 16; ++j) xb_st0(&bar[XB_XSUBI(i - 1, j)]);
;     xb_st0(&bar[XB_TOPI(i - 1)]);
; template <int W> DEVINL void xcd_barrier_w(const XcdBarrier& b, const Params& P, XPre& X) {
;     ...
;         __builtin_amdgcn_fence(__ATOMIC_ACQUIRE, "agent");
;         asm volatile("s_waitcnt vmcnt(0)" ::: "memory");
;         if (blockIdx.x == 0 && (W - 1) >= 1) xb_reset_after(bar, (W - 1));
.LBB0_570:
	s_waitcnt vmcnt(0)
	v_readlane_b32 s2, v254, 2
	s_waitcnt vmcnt(0)
	v_readlane_b32 s3, v254, 3
	s_andn2_b64 vcc, exec, s[2:3]
	s_cbranch_vccnz .LBB0_572
	s_getpc_b64 s[2:3]
	s_add_u32 s2, s2, g_xbar@rel32@lo+20484
	s_addc_u32 s3, s3, g_xbar@rel32@hi+20492
	v_mov_b32_e32 v1, 0
	global_store_dword v1, v1, s[2:3] sc1
	s_getpc_b64 s[2:3]
	s_add_u32 s2, s2, g_xbar@rel32@lo+20740
	s_addc_u32 s3, s3, g_xbar@rel32@hi+20748
	global_store_dword v1, v1, s[2:3] sc1
	s_getpc_b64 s[2:3]
	s_add_u32 s2, s2, g_xbar@rel32@lo+20996
	s_addc_u32 s3, s3, g_xbar@rel32@hi+21004
	global_store_dword v1, v1, s[2:3] sc1
	s_getpc_b64 s[2:3]
	s_add_u32 s2, s2, g_xbar@rel32@lo+21252
	s_addc_u32 s3, s3, g_xbar@rel32@hi+21260
	global_store_dword v1, v1, s[2:3] sc1
	s_getpc_b64 s[2:3]
	s_add_u32 s2, s2, g_xbar@rel32@lo+21508
	s_addc_u32 s3, s3, g_xbar@rel32@hi+21516
	global_store_dword v1, v1, s[2:3] sc1
	s_getpc_b64 s[2:3]
	s_add_u32 s2, s2, g_xbar@rel32@lo+21764
	s_addc_u32 s3, s3, g_xbar@rel32@hi+21772
	global_store_dword v1, v1, s[2:3] sc1
	s_getpc_b64 s[2:3]
	s_add_u32 s2, s2, g_xbar@rel32@lo+22020
	s_addc_u32 s3, s3, g_xbar@rel32@hi+22028
	global_store_dword v1, v1, s[2:3] sc1
	s_getpc_b64 s[2:3]
	s_add_u32 s2, s2, g_xbar@rel32@lo+22276
	s_addc_u32 s3, s3, g_xbar@rel32@hi+22284
	global_store_dword v1, v1, s[2:3] sc1
	s_getpc_b64 s[2:3]
	s_add_u32 s2, s2, g_xbar@rel32@lo+22532
	s_addc_u32 s3, s3, g_xbar@rel32@hi+22540
	global_store_dword v1, v1, s[2:3] sc1
	s_getpc_b64 s[2:3]
	s_add_u32 s2, s2, g_xbar@rel32@lo+22788
	s_addc_u32 s3, s3, g_xbar@rel32@hi+22796
	global_store_dword v1, v1, s[2:3] sc1
	s_getpc_b64 s[2:3]
	s_add_u32 s2, s2, g_xbar@rel32@lo+23044
	s_addc_u32 s3, s3, g_xbar@rel32@hi+23052
	global_store_dword v1, v1, s[2:3] sc1
	s_getpc_b64 s[2:3]
	s_add_u32 s2, s2, g_xbar@rel32@lo+23300
	s_addc_u32 s3, s3, g_xbar@rel32@hi+23308
	global_store_dword v1, v1, s[2:3] sc1
	s_getpc_b64 s[2:3]
	s_add_u32 s2, s2, g_xbar@rel32@lo+23556
	s_addc_u32 s3, s3, g_xbar@rel32@hi+23564
	global_store_dword v1, v1, s[2:3] sc1
	s_getpc_b64 s[2:3]
	s_add_u32 s2, s2, g_xbar@rel32@lo+23812
	s_addc_u32 s3, s3, g_xbar@rel32@hi+23820
	global_store_dword v1, v1, s[2:3] sc1
	s_getpc_b64 s[2:3]
	s_add_u32 s2, s2, g_xbar@rel32@lo+24068
	s_addc_u32 s3, s3, g_xbar@rel32@hi+24076
	global_store_dword v1, v1, s[2:3] sc1
	s_getpc_b64 s[2:3]
	s_add_u32 s2, s2, g_xbar@rel32@lo+24324
	s_addc_u32 s3, s3, g_xbar@rel32@hi+24332
	global_store_dword v1, v1, s[2:3] sc1
	s_getpc_b64 s[2:3]
	s_add_u32 s2, s2, g_xbar@rel32@lo+33028
	s_addc_u32 s3, s3, g_xbar@rel32@hi+33036
	global_store_dword v1, v1, s[2:3] sc1

; DEVINL unsigned xb_ld(unsigned* p)              { return __hip_atomic_load(p, __ATOMIC_RELAXED, __HIP_MEMORY_SCOPE_AGENT); }
; DEVINL unsigned xb_add(unsigned* p, unsigned v) { return __hip_atomic_fetch_add(p, v, __ATOMIC_RELAXED, __HIP_MEMORY_SCOPE_AGENT); }
; #define XB_SPIN(cond, bar) do { unsigned _sp = 0; while (cond) { __builtin_amdgcn_s_sleep(1); \
;     if ((++_sp & 255u) == 0u) { if (xb_ld(&(bar)[XB_TMO])) break; if (_sp > XB_SPIN_CAP) { atomicAdd(&(bar)[XB_TMO], 1u); break; } } } } while (0)
; DEVINL void xcd_barrier(const XcdBarrier& b, const int bi) {
;     ...
;     if (threadIdx.x == 0) {
;         unsigned* bar = b.bar;
;         __builtin_amdgcn_s_waitcnt(0);
;         unsigned nloc = b.st[0], nx = b.st[1];
;         const unsigned old = xb_add(&bar[XB_XSUBI(bi, b.x)], 1u);
;         if (nloc == 0u) { xcd_barrier_complete(bar, b.x, nloc, nx); b.st[0] = nloc; b.st[1] = nx; }
;         if (old + 1u == nloc) {
;             __builtin_amdgcn_fence(__ATOMIC_RELEASE, "agent");
;             asm volatile("s_waitcnt vmcnt(0)" ::: "memory");
;             (void)xb_add(&bar[XB_TOPI(bi)], 1u);
;         }
;         XB_SPIN(xb_ld(&bar[XB_TOPI(bi)]) < nx, bar);
.LBB0_663:
	s_or_b64 exec, exec, s[6:7]
	buffer_inv sc1
	v_mov_b32_e32 v1, 0
	s_getpc_b64 s[2:3]
	s_add_u32 s2, s2, g_xbar@rel32@lo+33540
	s_addc_u32 s3, s3, g_xbar@rel32@hi+33548
	global_load_dword v3, v1, s[2:3] sc1
	s_waitcnt vmcnt(0) lgkmcnt(0)
	v_cmp_ge_u32_e32 vcc, v3, v2
	s_cbranch_vccnz .LBB0_676
	s_mov_b32 s2, 1
	s_branch .LBB0_666

; DEVINL void xb_st0(unsigned* p) { __hip_atomic_store(p, 0u, __ATOMIC_RELAXED, __HIP_MEMORY_SCOPE_AGENT); }
; DEVINL void xb_reset_after(unsigned* bar, int i) {
; #pragma unroll
;     for (int j = 0; j < 16; ++j) xb_st0(&bar[XB_XSUBI(i - 1, j)]);
;     xb_st0(&bar[XB_TOPI(i - 1)]);
; DEVINL void xcd_barrier(const XcdBarrier& b, const int bi) {
;     ...
;         __builtin_amdgcn_fence(__ATOMIC_ACQUIRE, "agent");
;         asm volatile("s_waitcnt vmcnt(0)" ::: "memory");
;         if (blockIdx.x == 0 && bi >= 1) xb_reset_after(bar, bi);
.LBB0_676:
	s_waitcnt vmcnt(0)
	v_readlane_b32 s2, v254, 2
	s_waitcnt vmcnt(0)
	v_readlane_b32 s3, v254, 3
	s_andn2_b64 vcc, exec, s[2:3]
	s_cbranch_vccnz .LBB0_678
	s_getpc_b64 s[2:3]
	s_add_u32 s2, s2, g_xbar@rel32@lo+24580
	s_addc_u32 s3, s3, g_xbar@rel32@hi+24588
	v_mov_b32_e32 v1, 0
	global_store_dword v1, v1, s[2:3] sc1
	s_getpc_b64 s[2:3]
	s_add_u32 s2, s2, g_xbar@rel32@lo+24836
	s_addc_u32 s3, s3, g_xbar@rel32@hi+24844
	global_store_dword v1, v1, s[2:3] sc1
	s_getpc_b64 s[2:3]
	s_add_u32 s2, s2, g_xbar@rel32@lo+25092
	s_addc_u32 s3, s3, g_xbar@rel32@hi+25100
	global_store_dword v1, v1, s[2:3] sc1
	s_getpc_b64 s[2:3]
	s_add_u32 s2, s2, g_xbar@rel32@lo+25348
	s_addc_u32 s3, s3, g_xbar@rel32@hi+25356
	global_store_dword v1, v1, s[2:3] sc1
	s_getpc_b64 s[2:3]
	s_add_u32 s2, s2, g_xbar@rel32@lo+25604
	s_addc_u32 s3, s3, g_xbar@rel32@hi+25612
	global_store_dword v1, v1, s[2:3] sc1
	s_getpc_b64 s[2:3]
	s_add_u32 s2, s2, g_xbar@rel32@lo+25860
	s_addc_u32 s3, s3, g_xbar@rel32@hi+25868
	global_store_dword v1, v1, s[2:3] sc1
	s_getpc_b64 s[2:3]
	s_add_u32 s2, s2, g_xbar@rel32@lo+26116
	s_addc_u32 s3, s3, g_xbar@rel32@hi+26124
	global_store_dword v1, v1, s[2:3] sc1
	s_getpc_b64 s[2:3]
	s_add_u32 s2, s2, g_xbar@rel32@lo+26372
	s_addc_u32 s3, s3, g_xbar@rel32@hi+26380
	global_store_dword v1, v1, s[2:3] sc1
	s_getpc_b64 s[2:3]
	s_add_u32 s2, s2, g_xbar@rel32@lo+26628
	s_addc_u32 s3, s3, g_xbar@rel32@hi+26636
	global_store_dword v1, v1, s[2:3] sc1
	s_getpc_b64 s[2:3]
	s_add_u32 s2, s2, g_xbar@rel32@lo+26884
	s_addc_u32 s3, s3, g_xbar@rel32@hi+26892
	global_store_dword v1, v1, s[2:3] sc1
	s_getpc_b64 s[2:3]
	s_add_u32 s2, s2, g_xbar@rel32@lo+27140
	s_addc_u32 s3, s3, g_xbar@rel32@hi+27148
	global_store_dword v1, v1, s[2:3] sc1
	s_getpc_b64 s[2:3]
	s_add_u32 s2, s2, g_xbar@rel32@lo+27396
	s_addc_u32 s3, s3, g_xbar@rel32@hi+27404
	global_store_dword v1, v1, s[2:3] sc1
	s_getpc_b64 s[2:3]
	s_add_u32 s2, s2, g_xbar@rel32@lo+27652
	s_addc_u32 s3, s3, g_xbar@rel32@hi+27660
	global_store_dword v1, v1, s[2:3] sc1
	s_getpc_b64 s[2:3]
	s_add_u32 s2, s2, g_xbar@rel32@lo+27908
	s_addc_u32 s3, s3, g_xbar@rel32@hi+27916
	global_store_dword v1, v1, s[2:3] sc1
	s_getpc_b64 s[2:3]
	s_add_u32 s2, s2, g_xbar@rel32@lo+28164
	s_addc_u32 s3, s3, g_xbar@rel32@hi+28172
	global_store_dword v1, v1, s[2:3] sc1
	s_getpc_b64 s[2:3]
	s_add_u32 s2, s2, g_xbar@rel32@lo+28420
	s_addc_u32 s3, s3, g_xbar@rel32@hi+28428
	global_store_dword v1, v1, s[2:3] sc1
	s_getpc_b64 s[2:3]
	s_add_u32 s2, s2, g_xbar@rel32@lo+33284
	s_addc_u32 s3, s3, g_xbar@rel32@hi+33292
	global_store_dword v1, v1, s[2:3] sc1

; DEVINL void phase5(const Params& P, unsigned char* smem) {
;     ...
;     const int G = gridDim.x, vb = (G % 8 == 0) ? (int)(blockIdx.x % 8) * (G / 8) + (int)(blockIdx.x / 8) : (int)blockIdx.x;
;     typedef int i32x8 __attribute__((ext_vector_type(8)));
;     typedef int i32x4v __attribute__((ext_vector_type(4)));
;     ...
;     for (int it = vb; it < total; it += G) {
.LBB0_689:
	s_and_b32 s0, s80, 7
	s_ashr_i32 s1, s2, 3
	s_add_i32 s60, s3, 7
	s_lshr_b32 s60, s60, 3
	s_min_u32 s1, s1, s60
	s_mul_i32 s0, s1, s0
	s_lshr_b32 s61, s80, 3
	s_add_i32 s80, s0, s61
	s_cmp_ge_u32 s61, s1
	s_cbranch_scc1 .LBB0_744
	s_cmp_ge_i32 s80, s3
	s_cbranch_scc1 .LBB0_744

; DEVINL void phase5(const Params& P, unsigned char* smem) {
;     ...
;         __syncthreads();
;         {
; #pragma unroll
;             for (int rp = 0; rp < 2; ++rp) {
;                 const int row = (t >> 3) + 64 * rp, r = rbeg + row;
;                 if (row < 80) {
;                     const bool ok = r < rend;
;                     const int tok = ok ? ctok[cls * NT + r] : 0; const f32x2 w2 = ok ? cw[cls * NT + r] : (f32x2){0.f, 0.f};
;                     if ((t & 7) == 0) { s_tok[row] = ok ? tok : -1; s_wl[row] = w2.x; s_wh[row] = w2.y; }
;                     const unsigned char* src = H2 + (size_t)tok * DM;
; #pragma unroll
;                     for (int i = 0; i < 8; ++i) { const int c = (t & 7) + 8 * i; *(u32x4*)(smem + row * 1024 + ((c ^ (row & 15)) << 4)) = *(const u32x4*)(src + c * 16); }
;                 }
;             }
;         }
.LBB0_704:
	s_sub_i32 s29, s29, s28
	s_abs_i32 s30, s29
	v_cvt_f32_u32_e32 v2, s30
	s_add_i32 s31, s1, s29
	s_add_i32 s49, s31, -1
	s_sub_i32 s31, 1, s31
	v_rcp_iflag_f32_e32 v2, v2
	s_sub_i32 s51, 0, s30
	s_xor_b32 s29, s49, s29
	s_max_i32 s31, s49, s31
	v_mul_f32_e32 v2, 0x4f7ffffe, v2
	v_cvt_u32_f32_e32 v2, v2
	s_sub_i32 s28, s80, s28
	s_ashr_i32 s29, s29, 31
	v_mov_b32_e32 v34, v0
	v_readfirstlane_b32 s49, v2
	s_mul_i32 s51, s51, s49
	s_mul_hi_u32 s51, s49, s51
	s_add_i32 s49, s49, s51
	s_mul_hi_u32 s49, s31, s49
	s_mul_i32 s51, s49, s30
	s_sub_i32 s31, s31, s51
	s_add_i32 s52, s49, 1
	s_sub_i32 s51, s31, s30
	s_cmp_ge_u32 s31, s30
	s_cselect_b32 s49, s52, s49
	s_cselect_b32 s31, s51, s31
	s_add_i32 s51, s49, 1
	s_cmp_ge_u32 s31, s30
	s_cselect_b32 s30, s51, s49
	s_xor_b32 s30, s30, s29
	s_sub_i32 s29, s30, s29
	s_mul_i32 s49, s29, s28
	s_add_i32 s28, s49, s29
	s_min_i32 s51, s28, s1
	v_and_b32_e32 v223, 63, v34
	v_ashrrev_i32_e32 v12, 3, v34
	v_and_b32_e32 v10, 7, v34
	v_lshlrev_b32_e32 v194, 5, v223
	s_lshl_b32 s52, s0, 14
	v_cmp_eq_u32_e32 vcc, 0, v10
	v_and_b32_e32 v11, 15, v12
	v_cmp_gt_i32_e64 s[0:1], s43, v12
	s_barrier
	v_mov_b32_e32 v146, v10
	v_mov_b32_e32 v147, v11
	v_mov_b32_e32 v148, v12
	v_add_u32_e32 v50, s49, v148
	s_add_i32 s94, s51, -1
	v_add_u32_e32 v51, 64, v50
	v_cmp_gt_i32_e64 s[82:83], s51, v50
	v_min_i32_e32 v52, s94, v50
	v_min_i32_e32 v53, s94, v51
	v_cmp_gt_i32_e64 s[86:87], s51, v51
	v_add_u32_e32 v52, s52, v52
	v_add_u32_e32 v53, s52, v53
	v_lshlrev_b32_e32 v60, 2, v52
	v_lshlrev_b32_e32 v61, 2, v53
	v_lshlrev_b32_e32 v62, 3, v52
	v_lshlrev_b32_e32 v63, 3, v53
	global_load_dword v54, v60, s[6:7]
	global_load_dword v55, v61, s[6:7]
	global_load_dwordx2 v[56:57], v62, s[8:9]
	global_load_dwordx2 v[58:59], v63, s[8:9]
	v_readfirstlane_b32 s95, v148
	v_lshl_add_u32 v130, v148, 10, 0
	v_xor_b32_e32 v131, v147, v146
	v_bitop3_b32 v132, v146, v147, 8 bitop3:0x36
	v_bitop3_b32 v133, v146, v147, 16 bitop3:0x36
	v_bitop3_b32 v134, v146, v147, 24 bitop3:0x36
	v_bitop3_b32 v135, v146, v147, 32 bitop3:0x36
	v_bitop3_b32 v136, v146, v147, 40 bitop3:0x36
	v_bitop3_b32 v137, v146, v147, 48 bitop3:0x36
	v_bitop3_b32 v138, v146, v147, 56 bitop3:0x36
	v_lshl_add_u32 v131, v131, 4, v130
	v_lshl_add_u32 v132, v132, 4, v130
	v_lshl_add_u32 v133, v133, 4, v130
	v_lshl_add_u32 v134, v134, 4, v130
	v_lshl_add_u32 v135, v135, 4, v130
	v_lshl_add_u32 v136, v136, 4, v130
	v_lshl_add_u32 v137, v137, 4, v130
	v_lshl_add_u32 v138, v138, 4, v130
	v_lshl_add_u32 v140, v148, 2, 0
	v_cmp_eq_u32_e64 s[90:91], 0, v146
	v_cmp_gt_i32_e64 s[92:93], 16, v148
	s_waitcnt vmcnt(2)
	v_lshlrev_b32_e32 v64, 10, v54
	v_lshlrev_b32_e32 v65, 10, v55
	v_lshl_or_b32 v64, v146, 4, v64
	v_lshl_or_b32 v65, v146, 4, v65
	global_load_dwordx4 v[66:69], v64, s[4:5]
	global_load_dwordx4 v[70:73], v64, s[4:5] offset:128
	global_load_dwordx4 v[74:77], v64, s[4:5] offset:256
	global_load_dwordx4 v[78:81], v64, s[4:5] offset:384
	global_load_dwordx4 v[82:85], v64, s[4:5] offset:512
	global_load_dwordx4 v[86:89], v64, s[4:5] offset:640
	global_load_dwordx4 v[90:93], v64, s[4:5] offset:768
	global_load_dwordx4 v[94:97], v64, s[4:5] offset:896
	s_cmp_lt_u32 s95, 16
	s_cbranch_scc0 .Lp5_g_norows1
	global_load_dwordx4 v[98:101], v65, s[4:5]
	global_load_dwordx4 v[102:105], v65, s[4:5] offset:128
	global_load_dwordx4 v[106:109], v65, s[4:5] offset:256
	global_load_dwordx4 v[110:113], v65, s[4:5] offset:384
	global_load_dwordx4 v[114:117], v65, s[4:5] offset:512
	global_load_dwordx4 v[118:121], v65, s[4:5] offset:640
	global_load_dwordx4 v[122:125], v65, s[4:5] offset:768
	global_load_dwordx4 v[126:129], v65, s[4:5] offset:896
.Lp5_g_norows1:
	v_cndmask_b32_e64 v141, -1, v54, s[82:83]
	v_cndmask_b32_e64 v142, -1, v55, s[86:87]
	s_waitcnt vmcnt(0)
	v_cndmask_b32_e64 v56, 0, v56, s[82:83]
	v_cndmask_b32_e64 v57, 0, v57, s[82:83]
	v_cndmask_b32_e64 v58, 0, v58, s[86:87]
	v_cndmask_b32_e64 v59, 0, v59, s[86:87]
	ds_write_b128 v131, v[66:69]
	ds_write_b128 v132, v[70:73]
	ds_write_b128 v133, v[74:77]
	ds_write_b128 v134, v[78:81]
	ds_write_b128 v135, v[82:85]
	ds_write_b128 v136, v[86:89]
	ds_write_b128 v137, v[90:93]
	ds_write_b128 v138, v[94:97]
	s_mov_b64 s[82:83], exec
	s_and_b64 exec, s[82:83], s[90:91]
	v_add_u32_e32 v143, 0x24900, v140
	v_add_u32_e32 v144, 0x24a40, v140
	v_add_u32_e32 v145, 0x24b80, v140
	ds_write_b32 v143, v141
	ds_write_b32 v144, v56
	ds_write_b32 v145, v57
	s_and_b64 exec, exec, s[92:93]
	ds_write_b32 v143, v142 offset:256
	ds_write_b32 v144, v58 offset:256
	ds_write_b32 v145, v59 offset:256
	s_and_b64 exec, s[82:83], s[92:93]
	s_cbranch_execz .Lp5_g_skipw1
	v_add_u32_e32 v131, 0x10000, v131
	v_add_u32_e32 v132, 0x10000, v132
	v_add_u32_e32 v133, 0x10000, v133
	v_add_u32_e32 v134, 0x10000, v134
	v_add_u32_e32 v135, 0x10000, v135
	v_add_u32_e32 v136, 0x10000, v136
	v_add_u32_e32 v137, 0x10000, v137
	v_add_u32_e32 v138, 0x10000, v138
	ds_write_b128 v131, v[98:101]
	ds_write_b128 v132, v[102:105]
	ds_write_b128 v133, v[106:109]
	ds_write_b128 v134, v[110:113]
	ds_write_b128 v135, v[114:117]
	ds_write_b128 v136, v[118:121]
	ds_write_b128 v137, v[122:125]
	ds_write_b128 v138, v[126:129]
.Lp5_g_skipw1:
	s_mov_b64 exec, s[82:83]
